# W1 conversion split by blockIdx bit2 (XCDs 4-7 convert first)
# speedup vs baseline: 1.0066x; 1.0002x over previous
; #define LAS __attribute__((address_space(3)))
; #define REP(n) for (int rep_ = 0; rep_ < 1 + ((REPMASK >> (n)) & 1); ++rep_)
; #define IN(k) (lo <= (k) && (k) < hi && ((F = make_frame((LAS unsigned char*)lds_raw, wv)), true))
; #define SEAM(k) do { if ((k) + 1 < hi) xcd_barrier(bar, tid_now(wv) == 0); } while (0)
; DI void phase_expert_weights(const Frame& F, int l, int which) {
;     LAS float* scr = (LAS float*)(F.lds + F.wave * 16384);
;     unsigned char* ws = F.ws;
;     if (which == 0) {
;         constexpr int IPM = (D / 64) * (2048 / 32);
;         for (int it = F.gw; it < NE * IPM; it += F.NGW) { const int mtx = l * NE + it / IPM, r = it % IPM;
;             transpose_item(F.ap->in[32] + (size_t)mtx * D * 2048, D, 2048, (bf16_t*)(ws + WS_W1 + (size_t)mtx * 2048 * D), 3, scr, r, F.lane); }
; __global__ void __launch_bounds__(NTHR, 2) fwd_kernel(Args args) {
;     ...
;         REP(11) if (PM(11)) if (IN(pb + 8)) { phase_tail(F, l); SEAM(pb + 8); }
;         if (IN(pb + 9)) { phase_expert_weights(F, l, 0); SEAM(pb + 9); }
.LBB0_951:
	v_readlane_b32 s8, v253, 56
	v_readlane_b32 s9, v253, 57
	s_cmp_gt_i32 s96, s17
	s_mov_b32 s9, s29
	s_cselect_b64 s[4:5], -1, 0
	s_lshl_b32 s28, s8, 5
	v_writelane_b32 v253, s8, 56
	s_xor_b64 s[6:7], s[38:39], -1
	s_lshl_b64 s[48:49], s[8:9], 3
	v_writelane_b32 v253, s9, 57
	s_nop 0
	v_readlane_b32 s2, v253, 58
	s_or_b32 s17, s2, 11
	s_cmp_lt_i32 s17, s97
	s_cselect_b64 s[50:51], -1, 0
	s_or_b64 s[4:5], s[4:5], s[6:7]
	s_and_b64 vcc, exec, s[4:5]
	s_cbranch_vccnz .LBB0_1102
	s_bitcmp0_b32 s94, 2
	s_cbranch_scc1 .Lpre_skip
	s_mov_b32 s22, s10
	s_mov_b32 s23, s17
	s_mov_b64 s[24:25], s[38:39]
	v_mov_b32_e32 v42, v17
	s_mov_b64 s[4:5], s[58:59]
	v_readlane_b32 s2, v252, 0
	s_waitcnt lgkmcnt(0)
	v_mbcnt_lo_u32_b32 v0, -1, 0
	v_mbcnt_hi_u32_b32 v0, -1, v0
	s_mov_b32 s6, s94
	v_add_u32_e32 v1, s2, v0
	s_mov_b32 s2, s60
	s_and_b32 s7, s2, 7
	s_cmp_lg_u32 s7, 0
	v_readfirstlane_b32 s7, v1
	s_cbranch_scc1 .Lpre_1107
	s_ashr_i32 s9, s6, 31
	s_lshr_b32 s9, s9, 29
	s_add_i32 s9, s6, s9
	s_ashr_i32 s10, s9, 3
	s_and_b32 s9, s9, -8
	s_ashr_i32 s8, s2, 3
	s_sub_i32 s6, s6, s9
	s_mul_i32 s6, s8, s6
	s_add_i32 s6, s6, s10

; #define LAS __attribute__((address_space(3)))
; DI void phase_expert_weights(const Frame& F, int l, int which) {
;     LAS float* scr = (LAS float*)(F.lds + F.wave * 16384);
;     unsigned char* ws = F.ws;
;     if (which == 0) {
;         constexpr int IPM = (D / 64) * (2048 / 32);
;         for (int it = F.gw; it < NE * IPM; it += F.NGW) { const int mtx = l * NE + it / IPM, r = it % IPM;
;             transpose_item(F.ap->in[32] + (size_t)mtx * D * 2048, D, 2048, (bf16_t*)(ws + WS_W1 + (size_t)mtx * 2048 * D), 3, scr, r, F.lane); }
.LBB0_1104:
	v_readlane_b32 s50, v253, 50
	s_andn2_b64 vcc, exec, s[4:5]
	v_readlane_b32 s51, v253, 51
	s_cbranch_vccnz .LBB0_1160
	s_bitcmp1_b32 s94, 2
	s_cbranch_scc1 .LBB0_1110
	s_mov_b64 s[4:5], s[58:59]
	v_readlane_b32 s2, v252, 0
	s_waitcnt lgkmcnt(0)
	v_mbcnt_lo_u32_b32 v0, -1, 0
	v_mbcnt_hi_u32_b32 v0, -1, v0
	s_mov_b32 s6, s94
	v_add_u32_e32 v1, s2, v0
	s_mov_b32 s2, s60
	s_and_b32 s7, s2, 7
	s_cmp_lg_u32 s7, 0
	v_readfirstlane_b32 s7, v1
	s_cbranch_scc1 .LBB0_1107
	s_ashr_i32 s9, s6, 31
	s_lshr_b32 s9, s9, 29
	s_add_i32 s9, s6, s9
	s_ashr_i32 s10, s9, 3
	s_and_b32 s9, s9, -8
	s_ashr_i32 s8, s2, 3
	s_sub_i32 s6, s6, s9
	s_mul_i32 s6, s8, s6
	s_add_i32 s6, s6, s10
